# in-proj rope epilogue: dummy touch loads for later row groups rope-table lines right after group 0 loads (L2/L1 warm); plus in-proj weight prefetch
# speedup vs baseline: 1.0155x; 1.0027x over previous
.LBB0_3362:
	s_and_b64 s[4:5], s[6:7], exec
	s_cselect_b32 s4, s34, 0
	v_or_b32_e32 v132, s4, v250
	s_mov_b32 s4, 0x14e00000
	s_cselect_b32 s4, s4, 0x15600000
	s_add_u32 s62, s8, s4
	s_addc_u32 s63, s9, 0
	s_and_b64 s[4:5], s[6:7], exec
	v_lshlrev_b32_e32 v134, 3, v132
	v_mov_b32_e32 v135, v1
	v_cndmask_b32_e64 v131, 0, 1, s[64:65]
	s_cselect_b32 s66, 6, 5
	v_cmp_ne_u32_e64 s[4:5], 1, v131
	s_andn2_b64 vcc, exec, s[64:65]
	v_lshl_add_u64 v[134:135], s[62:63], 0, v[134:135]
	s_cbranch_vccnz .LBB0_3364
	v_ashrrev_i32_e32 v131, 31, v130
	v_lshlrev_b64 v[136:137], s66, v[130:131]
	v_lshl_add_u64 v[136:137], v[136:137], 3, v[134:135]
	global_load_dwordx4 v[158:161], v[136:137], off offset:48
	global_load_dwordx4 v[138:141], v[136:137], off offset:32
	global_load_dwordx4 v[142:145], v[136:137], off offset:16
	global_load_dwordx4 v[146:149], v[136:137], off
	s_add_i32 s98, s66, 7
	s_lshl_b32 s98, 1, s98
	s_mov_b32 s99, 0
	v_lshl_add_u64 v[210:211], v[136:137], 0, s[98:99]
	global_load_dword v212, v[210:211], off
	v_lshl_add_u64 v[210:211], v[210:211], 0, s[98:99]
	global_load_dword v212, v[210:211], off
	v_lshl_add_u64 v[210:211], v[210:211], 0, s[98:99]
	global_load_dword v212, v[210:211], off
	v_lshl_add_u64 v[210:211], v[210:211], 0, s[98:99]
	v_lshl_add_u64 v[210:211], v[210:211], 0, s[98:99]
	v_lshl_add_u64 v[210:211], v[210:211], 0, s[98:99]
	v_lshl_add_u64 v[210:211], v[210:211], 0, s[98:99]
	v_lshl_add_u64 v[210:211], v[210:211], 0, s[98:99]
	global_load_dword v212, v[210:211], off
	v_lshl_add_u64 v[210:211], v[210:211], 0, s[98:99]
	global_load_dword v212, v[210:211], off
	v_lshl_add_u64 v[210:211], v[210:211], 0, s[98:99]
	global_load_dword v212, v[210:211], off
	v_lshl_add_u64 v[210:211], v[210:211], 0, s[98:99]
	global_load_dword v212, v[210:211], off
	s_waitcnt vmcnt(0)
	v_mul_f32_e32 v164, v124, v158
	v_mov_b32_e32 v153, v140
	v_mov_b32_e32 v140, v139
	v_mov_b32_e32 v137, v148
	v_mov_b32_e32 v148, v147
	v_mov_b32_e32 v136, v146
	v_pk_mul_f32 v[162:163], v[118:119], v[148:149]
	v_pk_mul_f32 v[146:147], v[126:127], v[148:149]
	v_mov_b32_e32 v149, v144
	v_mov_b32_e32 v144, v143
	v_mov_b32_e32 v148, v142
	v_pk_mul_f32 v[142:143], v[120:121], v[144:145]
	v_pk_mul_f32 v[150:151], v[128:129], v[144:145]
	v_mov_b32_e32 v152, v138
	v_pk_mul_f32 v[138:139], v[114:115], v[140:141]
	v_pk_mul_f32 v[154:155], v[122:123], v[140:141]
	v_mov_b32_e32 v140, v125
	v_mov_b32_e32 v141, v117
	v_pk_fma_f32 v[144:145], v[126:127], v[136:137], v[162:163] neg_lo:[0,0,1] neg_hi:[0,0,1]
	v_mov_b32_e32 v162, v117
	v_mov_b32_e32 v163, v125
	v_pk_mul_f32 v[140:141], v[140:141], v[160:161]
	v_pk_mul_f32 v[160:161], v[162:163], v[160:161]
	v_mul_f32_e32 v166, v116, v159
	v_mul_f32_e32 v156, v116, v158
	v_mul_f32_e32 v158, v124, v159
	v_mov_b32_e32 v165, v140
	v_mov_b32_e32 v167, v141
	v_mov_b32_e32 v157, v160
	v_mov_b32_e32 v159, v161
	v_pk_fma_f32 v[142:143], v[128:129], v[148:149], v[142:143] neg_lo:[0,0,1] neg_hi:[0,0,1]
	v_pk_fma_f32 v[140:141], v[122:123], v[152:153], v[138:139] neg_lo:[0,0,1] neg_hi:[0,0,1]
	v_pk_add_f32 v[138:139], v[164:165], v[166:167] neg_lo:[0,1] neg_hi:[0,1]
	v_pk_fma_f32 v[160:161], v[118:119], v[136:137], v[146:147]
	v_pk_fma_f32 v[150:151], v[120:121], v[148:149], v[150:151]
	v_pk_fma_f32 v[148:149], v[114:115], v[152:153], v[154:155]
	v_pk_add_f32 v[146:147], v[156:157], v[158:159]
	s_branch .LBB0_3365

.LBB0_3481:
	s_and_b64 s[4:5], s[6:7], exec
	s_cselect_b32 s4, s94, 0
	v_or_b32_e32 v66, s4, v250
	s_mov_b32 s4, 0x14e00000
	s_cselect_b32 s4, s4, 0x15600000
	s_add_u32 s84, s8, s4
	s_addc_u32 s85, s9, 0
	s_and_b64 s[4:5], s[6:7], exec
	v_lshlrev_b32_e32 v68, 3, v66
	v_mov_b32_e32 v69, v1
	v_cndmask_b32_e64 v19, 0, 1, s[62:63]
	s_cselect_b32 s64, 6, 5
	v_cmp_ne_u32_e64 s[4:5], 1, v19
	s_andn2_b64 vcc, exec, s[62:63]
	v_lshl_add_u64 v[68:69], s[84:85], 0, v[68:69]
	s_cbranch_vccnz .LBB0_3483
	v_ashrrev_i32_e32 v19, 31, v18
	v_lshlrev_b64 v[70:71], s64, v[18:19]
	v_lshl_add_u64 v[70:71], v[70:71], 3, v[68:69]
	global_load_dwordx4 v[92:95], v[70:71], off offset:48
	global_load_dwordx4 v[72:75], v[70:71], off offset:32
	global_load_dwordx4 v[76:79], v[70:71], off offset:16
	global_load_dwordx4 v[80:83], v[70:71], off
	s_add_i32 s98, s64, 7
	s_lshl_b32 s98, 1, s98
	s_mov_b32 s99, 0
	v_lshl_add_u64 v[210:211], v[70:71], 0, s[98:99]
	global_load_dword v212, v[210:211], off
	v_lshl_add_u64 v[210:211], v[210:211], 0, s[98:99]
	global_load_dword v212, v[210:211], off
	v_lshl_add_u64 v[210:211], v[210:211], 0, s[98:99]
	global_load_dword v212, v[210:211], off
	v_lshl_add_u64 v[210:211], v[210:211], 0, s[98:99]
	v_lshl_add_u64 v[210:211], v[210:211], 0, s[98:99]
	v_lshl_add_u64 v[210:211], v[210:211], 0, s[98:99]
	v_lshl_add_u64 v[210:211], v[210:211], 0, s[98:99]
	v_lshl_add_u64 v[210:211], v[210:211], 0, s[98:99]
	global_load_dword v212, v[210:211], off
	v_lshl_add_u64 v[210:211], v[210:211], 0, s[98:99]
	global_load_dword v212, v[210:211], off
	v_lshl_add_u64 v[210:211], v[210:211], 0, s[98:99]
	global_load_dword v212, v[210:211], off
	v_lshl_add_u64 v[210:211], v[210:211], 0, s[98:99]
	global_load_dword v212, v[210:211], off
	s_waitcnt vmcnt(0)
	v_mul_f32_e32 v98, v188, v92
	v_mov_b32_e32 v87, v74
	v_mov_b32_e32 v74, v73
	v_mov_b32_e32 v71, v82
	v_mov_b32_e32 v82, v81
	v_mov_b32_e32 v70, v80
	v_pk_mul_f32 v[96:97], v[158:159], v[82:83]
	v_pk_mul_f32 v[80:81], v[190:191], v[82:83]
	v_mov_b32_e32 v83, v78
	v_mov_b32_e32 v78, v77
	v_mov_b32_e32 v82, v76
	v_pk_mul_f32 v[76:77], v[160:161], v[78:79]
	v_pk_mul_f32 v[84:85], v[192:193], v[78:79]
	v_mov_b32_e32 v86, v72
	v_pk_mul_f32 v[72:73], v[154:155], v[74:75]
	v_pk_mul_f32 v[88:89], v[186:187], v[74:75]
	v_mov_b32_e32 v74, v189
	v_mov_b32_e32 v75, v157
	v_pk_fma_f32 v[78:79], v[190:191], v[70:71], v[96:97] neg_lo:[0,0,1] neg_hi:[0,0,1]
	v_mov_b32_e32 v96, v157
	v_mov_b32_e32 v97, v189
	v_pk_mul_f32 v[74:75], v[74:75], v[94:95]
	v_pk_mul_f32 v[94:95], v[96:97], v[94:95]
	v_mul_f32_e32 v100, v156, v93
	v_mul_f32_e32 v90, v156, v92
	v_mul_f32_e32 v92, v188, v93
	v_mov_b32_e32 v99, v74
	v_mov_b32_e32 v101, v75
	v_mov_b32_e32 v91, v94
	v_mov_b32_e32 v93, v95
	v_pk_fma_f32 v[76:77], v[192:193], v[82:83], v[76:77] neg_lo:[0,0,1] neg_hi:[0,0,1]
	v_pk_fma_f32 v[74:75], v[186:187], v[86:87], v[72:73] neg_lo:[0,0,1] neg_hi:[0,0,1]
	v_pk_add_f32 v[72:73], v[98:99], v[100:101] neg_lo:[0,1] neg_hi:[0,1]
	v_pk_fma_f32 v[94:95], v[158:159], v[70:71], v[80:81]
	v_pk_fma_f32 v[84:85], v[160:161], v[82:83], v[84:85]
	v_pk_fma_f32 v[82:83], v[154:155], v[86:87], v[88:89]
	v_pk_add_f32 v[80:81], v[90:91], v[92:93]
	s_branch .LBB0_3484
